# in-proj and gate_up phase prologues: compiler-inserted vmcnt(0) between tile-0 and tile-1 staging relaxed to vmcnt(2) (row-partials load is older than the tile loads, already retired by the preceding
# speedup vs baseline: 1.0053x; 1.0053x over previous
; #define PG8_LAS __attribute__((address_space(3)))
;     __device__ bool next(int i, Unit& u) const { if (!base.next(i >> 1, u)) return false; if (i & 1) { u.pm += MTOK / BM; u.pn += DM / BM; } return true; }
; template <class Epi, class Sched, bool ALIGN_EPI = false, bool SP2 = false>
; __device__ __forceinline__ void gemm_phase(PG8_LAS unsigned char* lds, const Gemm g, const Sched& S, const Epi& E) {
;     ...
;     for (int i = 0; i < 2; ++i) { int R, C; stage_rc(tid * 16 + i * 8192, R, C); const int Rb = Epi::PERM ? ((R & ~31) + perm32(R & 31)) : R;
;         voffA[i] = (unsigned)(R * K + C) * 2u; voffB[i] = (unsigned)(Rb * K + C) * 2u; }
;     const size_t kstep = (size_t)(BK * 2);
;     const size_t hstep = (size_t)HALF * K * 2;
;     const size_t tstep = 2 * hstep;
;     const unsigned ldsw = (unsigned)wid * 1024u;
;     const int aoff = lds_byte(wr * 64 + fr, fq * 8), boff = lds_byte(wc * 32 + fr, fq * 8);
;     ...
;     Unit cur, nxt; int ui = 0;
;     ...
;     unsigned pg8_probe_acc = 0u;
;     ...
;     if (!S.next(0, cur)) return;
;     ...
;     const unsigned long long tramp_ = __builtin_amdgcn_s_memrealtime();
;     ...
;     static_assert(!Epi::ROWSCALE || SP2, "row factors are staged in the SP2 prologue");
;     f32x4 rowp_ = {0.f, 0.f, 0.f, 0.f}; if constexpr (Epi::ROWSCALE) rowp_ = load_row_partials(E.rsp, cur.pm, tid);
;     f32x4 acc[2][2][4][2];
; #pragma unroll
;     for (int a = 0; a < 2; ++a)
; #pragma unroll
;         for (int b = 0; b < 2; ++b)
; #pragma unroll
;             for (int m = 0; m < 4; ++m)
; #pragma unroll
;                 for (int n = 0; n < 2; ++n) acc[a][b][m][n] = (f32x4){0.f, 0.f, 0.f, 0.f};
;     bf16x8 At[4][2], B0[2][2], B1[2][2];
;     const char* cA = (const char*)g.A + (size_t)cur.pm * tstep + (cur.half == 2 ? hstep : (size_t)0); const char* cB = (const char*)g.Bt + (size_t)cur.pn * tstep;
;     S.a_ready(cur);
;     if constexpr (SP2) {
;         PG8_STAGE(PG8_SB(0, 0), cB, voffB); PG8_STAGE(PG8_SB(0, 1), cB + hstep, voffB); PG8_STAGE(PG8_SA(0, 0), cA, voffA); PG8_STAGE(PG8_SA(0, 1), cA + hstep, voffA);
;         if (wr == 1) PG8_BAR;
;         PG8_WAIT_V(2); PG8_BAR;
;         if constexpr (Epi::ROWSCALE) stage_row_factors(rowp_, (PG8_LAS float*)E.rsl, tid);
;         PG8_STAGE(PG8_SB(1, 0), cB + kstep, voffB); PG8_STAGE(PG8_SA(1, 0), cA + kstep, voffA); PG8_STAGE(PG8_SB(1, 1), cB + hstep + kstep, voffB);
;         PG8_WAIT_V(6); PG8_BAR;
.LBB0_385:
	s_or_b64 exec, exec, s[0:1]
	v_ashrrev_i32_e32 v9, 31, v2
	v_lshrrev_b32_e32 v9, 26, v9
	v_add_u32_e32 v9, v2, v9
	v_ashrrev_i32_e32 v16, 6, v9
	v_bfe_i32 v9, v2, 27, 1
	v_lshlrev_b32_e32 v8, 4, v2
	v_lshrrev_b32_e32 v9, 22, v9
	v_add_u32_e32 v9, v8, v9
	v_and_b32_e32 v9, 0xfffffc00, v9
	v_sub_u32_e32 v9, v8, v9
	v_lshrrev_b32_e32 v10, 4, v9
	v_bitop3_b32 v9, v10, v9, 32 bitop3:0x6c
	v_ashrrev_i32_e32 v11, 31, v9
	v_lshrrev_b32_e32 v11, 26, v11
	v_add_u32_e32 v11, v9, v11
	v_lshlrev_b32_e32 v10, 3, v16
	v_ashrrev_i32_e32 v17, 6, v11
	v_and_b32_e32 v11, 0xc0, v11
	v_and_b32_e32 v10, -16, v10
	v_sub_u32_e32 v9, v9, v11
	v_add_u32_e32 v10, v17, v10
	v_ashrrev_i16_sdwa v9, v224, sext(v9) dst_sel:DWORD dst_unused:UNUSED_PAD src0_sel:DWORD src1_sel:BYTE_0
	v_lshlrev_b32_e32 v12, 5, v16
	v_bfe_i32 v18, v9, 0, 16
	v_lshlrev_b32_e32 v9, 1, v10
	v_lshrrev_b32_e32 v11, 2, v10
	v_and_b32_e32 v13, 3, v17
	s_mov_b32 s0, 0x1fffe0
	v_and_b32_e32 v12, 32, v12
	v_and_b32_e32 v9, 24, v9
	v_and_b32_e32 v11, 4, v11
	v_and_or_b32 v13, v10, s0, v13
	v_or3_b32 v9, v13, v11, v9
	v_add_lshl_u32 v11, v12, v18, 1
	v_add_u32_e32 v8, 0x2000, v8
	v_lshl_add_u32 v166, v9, 11, v11
	v_ashrrev_i32_e32 v9, 31, v8
	v_lshrrev_b32_e32 v9, 22, v9
	v_add_u32_e32 v9, v8, v9
	v_ashrrev_i32_e32 v19, 10, v9
	v_mul_i32_i24_e32 v9, 0x400, v19
	v_sub_u32_e32 v8, v8, v9
	v_lshrrev_b32_e32 v9, 4, v8
	v_bitop3_b32 v8, v9, v8, 32 bitop3:0x6c
	v_lshl_add_u32 v164, v10, 11, v11
	v_ashrrev_i32_e32 v10, 31, v8
	v_lshrrev_b32_e32 v10, 26, v10
	v_lshlrev_b32_e32 v9, 3, v19
	v_add_u32_e32 v10, v8, v10
	s_add_u32 s24, s16, 0x14000000
	v_and_b32_e32 v9, -16, v9
	v_ashrrev_i32_e32 v20, 6, v10
	s_addc_u32 s25, s17, 0
	s_ashr_i32 s11, s10, 6
	v_add_u32_e32 v9, v20, v9
	v_and_b32_e32 v12, 3, v20
	s_mul_i32 s36, s77, 0xee0000
	v_and_or_b32 v12, v9, s0, v12
	s_ashr_i32 s26, s10, 8
	s_lshl_b32 s27, s11, 10
	s_lshl_b64 s[0:1], s[36:37], 1
	s_add_u32 s28, s22, s0
	v_and_b32_e32 v10, 0xc0, v10
	s_addc_u32 s29, s23, s1
	s_ashr_i32 s19, s18, 31
	s_ashr_i32 s71, s70, 31
	v_sub_u32_e32 v8, v8, v10
	s_lshl_b64 s[6:7], s[18:19], 19
	s_lshl_b64 s[0:1], s[70:71], 19
	v_ashrrev_i16_sdwa v8, v224, sext(v8) dst_sel:DWORD dst_unused:UNUSED_PAD src0_sel:DWORD src1_sel:BYTE_0
	s_add_u32 s0, s28, s0
	v_lshlrev_b32_e32 v11, 5, v19
	v_bfe_i32 v21, v8, 0, 16
	v_lshlrev_b32_e32 v8, 1, v9
	v_lshrrev_b32_e32 v10, 2, v9
	s_addc_u32 s1, s29, s1
	s_add_i32 s19, s27, 0
	v_and_b32_e32 v11, 32, v11
	v_and_b32_e32 v8, 24, v8
	v_and_b32_e32 v10, 4, v10
	s_add_i32 m0, s19, 0x10000
	v_or3_b32 v8, v12, v10, v8
	v_add_lshl_u32 v10, v11, v21, 1
	global_load_lds_dwordx4 v166, s[0:1]
	s_add_i32 m0, s19, 0x12000
	v_lshl_add_u32 v170, v8, 11, v10
	s_add_u32 s8, s0, 0x40000
	global_load_lds_dwordx4 v170, s[0:1]
	s_addc_u32 s9, s1, 0
	s_add_i32 m0, s19, 0x14000
	v_lshl_add_u32 v168, v9, 11, v10
	global_load_lds_dwordx4 v166, s[8:9]
	s_add_i32 m0, s19, 0x16000
	s_nop 0
	global_load_lds_dwordx4 v170, s[8:9]
	s_add_u32 s8, s24, s6
	s_addc_u32 s9, s25, s7
	s_add_i32 s30, s19, 0x2000
	s_mov_b32 m0, s19
	s_add_u32 s6, s8, 0x40000
	global_load_lds_dwordx4 v164, s[8:9]
	s_mov_b32 m0, s30
	s_addc_u32 s7, s9, 0
	s_add_i32 s31, s19, 0x4000
	global_load_lds_dwordx4 v168, s[8:9]
	s_mov_b32 m0, s31
	s_add_i32 s34, s19, 0x6000
	global_load_lds_dwordx4 v164, s[6:7]
	s_mov_b32 m0, s34
	s_cmp_eq_u32 s26, 1
	global_load_lds_dwordx4 v168, s[6:7]
	s_cselect_b64 s[56:57], -1, 0
	s_cmp_lg_u32 s26, 1
	s_cbranch_scc1 .LBB0_387
	s_barrier
.LBB0_387:
	s_waitcnt vmcnt(2)
	v_mov_b32_e32 v167, v3
	v_mov_b32_e32 v171, v3
	v_mov_b32_e32 v165, v3
	v_mov_b32_e32 v169, v3
	v_lshl_add_u64 v[12:13], s[0:1], 0, v[166:167]
	v_lshl_add_u64 v[14:15], s[0:1], 0, v[170:171]
	v_lshl_add_u64 v[10:11], s[8:9], 0, v[164:165]
	v_lshl_add_u64 v[8:9], s[8:9], 0, v[168:169]
	s_barrier
	s_and_saveexec_b64 s[6:7], s[4:5]
	s_cbranch_execz .LBB0_389
	s_waitcnt vmcnt(2)
	v_mov_b32_e32 v22, v5
	v_mov_b32_e32 v23, v6
	v_mov_b32_e32 v5, v7
	v_pk_add_f32 v[4:5], v[22:23], v[4:5]
	s_nop 0
	v_add_f32_e32 v4, v4, v5
	v_fmamk_f32 v4, v4, 0x3a800000, v226
	v_rsq_f32_e32 v4, v4
	v_lshl_add_u32 v5, v2, 2, 0
	v_add_u32_e32 v5, 0x20400, v5
	ds_write_b32 v5, v4
.LBB0_389:
	s_or_b64 exec, exec, s[6:7]
	s_add_u32 s35, s16, 0x500000
	s_addc_u32 s40, s17, 0
	s_and_b32 s12, s11, 3
	s_add_i32 m0, s19, 0x18000
	s_waitcnt vmcnt(2)
	v_lshl_add_u64 v[4:5], v[12:13], 0, s[42:43]
	s_lshl_b32 s6, s26, 13
	s_lshl_b32 s7, s12, 12
	global_load_lds_dwordx4 v[4:5], off
	v_lshl_add_u64 v[4:5], v[14:15], 0, s[42:43]
	s_add_i32 m0, s19, 0x1a000
	s_add_i32 s41, s19, 0x8000
	s_add_i32 s71, s19, 0xa000
	global_load_lds_dwordx4 v[4:5], off
	v_lshl_add_u64 v[4:5], v[10:11], 0, s[42:43]
	s_mov_b32 m0, s41
	s_add_u32 s4, s0, 0x40080
	global_load_lds_dwordx4 v[4:5], off
	v_lshl_add_u64 v[4:5], v[8:9], 0, s[42:43]
	s_mov_b32 m0, s71
	s_addc_u32 s5, s1, 0
	global_load_lds_dwordx4 v[4:5], off
	s_add_i32 m0, s19, 0x1c000
	v_lshl_add_u64 v[4:5], s[4:5], 0, v[166:167]
	global_load_lds_dwordx4 v[4:5], off
	v_lshl_add_u64 v[4:5], s[4:5], 0, v[170:171]
	s_add_i32 m0, s19, 0x1e000
	s_cmpk_lt_u32 s10, 0x100
	global_load_lds_dwordx4 v[4:5], off
	v_and_b32_e32 v4, 15, v2
	v_bfe_u32 v5, v2, 4, 2
	v_lshl_or_b32 v202, s26, 6, v4
	v_lshlrev_b32_e32 v7, 4, v5
	v_lshlrev_b32_e32 v8, 2, v202
	v_lshlrev_b32_e32 v2, 2, v2
	v_lshl_or_b32 v7, v4, 6, v7
	v_and_b32_e32 v9, 32, v8
	v_and_b32_e32 v2, 32, v2
	v_bitop3_b32 v9, v7, s6, v9 bitop3:0xde
	v_bitop3_b32 v203, v7, s7, v2 bitop3:0xde
	s_cselect_b64 s[58:59], -1, 0
	s_lshl_b32 s6, s11, 4
	v_lshlrev_b32_e32 v2, 2, v5
	v_and_or_b32 v204, s6, 16, v2
	s_lshl_b32 s10, s12, 1
	s_or_b32 s74, s10, -16
	s_add_i32 s10, 0, 0x20400
	v_lshlrev_b32_e32 v2, 2, v204
	v_lshlrev_b32_e32 v6, 3, v5
	v_cmp_eq_u32_e64 s[4:5], 0, v5
	s_bfe_u32 s73, s11, 0x10001
	v_cmp_eq_u32_e64 s[6:7], 0, v4
	v_add_u32_e32 v205, s10, v8
	v_lshl_add_u64 v[4:5], s[16:17], 0, v[2:3]
	s_mov_b64 s[10:11], 0x100000
	v_lshlrev_b32_e32 v2, 14, v16
	v_lshl_add_u64 v[174:175], v[4:5], 0, s[10:11]
	s_mov_b64 s[10:11], 0x300000
	v_and_b32_e32 v2, 0xffff8000, v2
	v_lshl_add_u64 v[176:177], v[4:5], 0, s[10:11]
	v_lshl_add_u32 v2, v17, 11, v2
	v_and_b32_e32 v4, 1, v16
	v_lshl_or_b32 v2, v4, 6, v2
	v_lshl_add_u32 v178, v18, 1, v2
	v_lshlrev_b32_e32 v2, 14, v19
	v_and_b32_e32 v2, 0xffff8000, v2
	s_waitcnt vmcnt(6)
	v_lshl_add_u32 v2, v20, 11, v2
	v_and_b32_e32 v4, 1, v19
	s_add_u32 s75, s16, 0xf000000
	v_lshl_or_b32 v2, v4, 6, v2
	v_lshl_or_b32 v172, s12, 5, v6
	v_mov_b32_e32 v173, v3
	s_mov_b32 s72, 0
	s_addc_u32 s76, s17, 0
	v_mov_b32_e32 v179, v3
	v_lshl_add_u32 v180, v21, 1, v2
	v_mov_b32_e32 v181, v3
	v_add_u32_e32 v206, 0, v9
	s_barrier
	s_branch .LBB0_392

;     __device__ __forceinline__ void a_ready(const Unit&) const { if (++ncall == 3 && sig != nullptr && threadIdx.x == 0) __hip_atomic_fetch_add(sig, 1u, __ATOMIC_RELAXED, __HIP_MEMORY_SCOPE_AGENT); }
; #define PG8_STAGE(bufoff, gbase, voff) do { _Pragma("unroll") for (int _i = 0; _i < 2; ++_i) \
;         __builtin_amdgcn_global_load_lds((const unsigned*)((const char*)(gbase) + (voff)[_i]), (PG8_LAS unsigned*)(lds + (bufoff) + ldsw + _i * 8192), 16, 0, 0); } while (0)
; #define PG8_LDA(dst, b, h) do { _Pragma("unroll") for (int m = 0; m < 4; ++m) _Pragma("unroll") for (int k = 0; k < 2; ++k) dst[m][k] = *(const PG8_LAS bf16x8*)(lds + PG8_SA(b, h) + aoff + m * 2048 + k * 1024); } while (0)
; #define PG8_LDB(dst, b, h) do { _Pragma("unroll") for (int n = 0; n < 2; ++n) _Pragma("unroll") for (int k = 0; k < 2; ++k) dst[n][k] = *(const PG8_LAS bf16x8*)(lds + PG8_SB(b, h) + boff + n * 2048 + k * 1024); } while (0)
; #define PG8_WAIT_V(n) asm volatile("s_waitcnt vmcnt(" #n ")" ::: "memory")
; template <class Epi, class Sched, bool ALIGN_EPI = false, bool SP2 = false>
; __device__ __forceinline__ void gemm_phase(PG8_LAS unsigned char* lds, const Gemm g, const Sched& S, const Epi& E) {
;     ...
;         for (int t = 0; t < nt; t += 2) {
;             const bool last = (t == nt - 2);
;             const char* a1 = cA + (size_t)(t + 1) * kstep;
;             const char* a2 = last ? nA : cA + (size_t)(t + 2) * kstep; const char* b2 = last ? nB : cB + (size_t)(t + 2) * kstep;
;             const char* a3 = a2 + kstep; const char* b3 = b2 + kstep;
;             if (last && has_next) S.a_ready(nxt);
;             if constexpr (SP2) {
;             PG8_LDB(B0, 0, 0); PG8_LDB(B1, 0, 1); PG8_SCHED; PG8_LDA(At, 0, 0); PG8_STAGE(PG8_SA(1, 1), a1 + hstep, voffA);
;     ...
;             if (PROBE_KIND == 18 && t == 0 && ui > 0 && g.probe) { const unsigned long long tq_ = __builtin_amdgcn_s_memrealtime(); PG8_WAIT_V(8); pg8_probe_acc += (unsigned)(__builtin_amdgcn_s_memrealtime() - tq_); }
;     ...
;             PG8_WAIT_V(8); PG8_WAIT_L(0); PG8_BAR; PG8_MMA(0, 0, At, B0); PG8_MMA(0, 1, At, B1); PG8_BAR; PG8_SCHED;
;             PG8_LDA(At, 0, 1); PG8_STAGE(PG8_SB(0, 0), b2, voffB); PG8_STAGE(PG8_SB(0, 1), b2 + hstep, voffB); PG8_STAGE(PG8_SA(0, 0), a2, voffA);
;             PG8_WAIT_V(8); PG8_WAIT_L(0); PG8_BAR; if (cur.half == 0) { PG8_MMA(1, 0, At, B0); PG8_MMA(1, 1, At, B1); } PG8_BAR; PG8_SCHED;
.LBB0_395:
	s_add_u32 s0, s8, 0xfffc0080
	s_addc_u32 s1, s9, -1
	s_add_i32 s61, 0, 0x10000
	s_cmp_eq_u32 s39, 12
	s_cselect_b32 s11, s12, s1
	s_cselect_b32 s10, s13, s0
	v_add_u32_e32 v2, s61, v203
	s_cselect_b32 s1, s14, s38
	s_cselect_b32 s0, s15, s36
	s_add_i32 s63, 0, 0x14000
	ds_read_b128 v[132:135], v2
	ds_read_b128 v[136:139], v2 offset:1024
	ds_read_b128 v[140:143], v2 offset:2048
	ds_read_b128 v[144:147], v2 offset:3072
	v_add_u32_e32 v2, s63, v203
	ds_read_b128 v[148:151], v2
	ds_read_b128 v[152:155], v2 offset:1024
	ds_read_b128 v[156:159], v2 offset:2048
	ds_read_b128 v[160:163], v2 offset:3072
	v_lshl_add_u64 v[228:229], s[8:9], 0, v[178:179]
	s_add_i32 m0, s19, 0xc000
	ds_read_b128 v[182:185], v206
	ds_read_b128 v[186:189], v206 offset:1024
	ds_read_b128 v[190:193], v206 offset:2048
	ds_read_b128 v[194:197], v206 offset:3072
	ds_read_b128 v[198:201], v206 offset:4096
	ds_read_b128 v[208:211], v206 offset:5120
	ds_read_b128 v[212:215], v206 offset:6144
	ds_read_b128 v[216:219], v206 offset:7168
	global_load_lds_dwordx4 v[228:229], off
	v_lshl_add_u64 v[228:229], s[8:9], 0, v[180:181]
	s_add_i32 m0, s19, 0xe000
	s_nop 0
	global_load_lds_dwordx4 v[228:229], off
	s_waitcnt vmcnt(8)
	s_waitcnt lgkmcnt(0)
	s_barrier
	s_setprio 1
	s_waitcnt lgkmcnt(0)
	v_mfma_f32_16x16x32_bf16 v[128:131], v[132:135], v[182:185], v[128:131]
	v_mfma_f32_16x16x32_bf16 v[124:127], v[140:143], v[182:185], v[124:127]
	v_mfma_f32_16x16x32_bf16 v[112:115], v[132:135], v[190:193], v[112:115]
	v_mfma_f32_16x16x32_bf16 v[108:111], v[140:143], v[190:193], v[108:111]
	v_mfma_f32_16x16x32_bf16 v[96:99], v[132:135], v[198:201], v[96:99]
	v_mfma_f32_16x16x32_bf16 v[92:95], v[140:143], v[198:201], v[92:95]
	v_mfma_f32_16x16x32_bf16 v[80:83], v[132:135], v[212:215], v[80:83]
	v_mfma_f32_16x16x32_bf16 v[76:79], v[140:143], v[212:215], v[76:79]
	v_mfma_f32_16x16x32_bf16 v[128:131], v[136:139], v[186:189], v[128:131]
	v_mfma_f32_16x16x32_bf16 v[124:127], v[144:147], v[186:189], v[124:127]
	v_mfma_f32_16x16x32_bf16 v[112:115], v[136:139], v[194:197], v[112:115]
	v_mfma_f32_16x16x32_bf16 v[108:111], v[144:147], v[194:197], v[108:111]
	v_mfma_f32_16x16x32_bf16 v[96:99], v[136:139], v[208:211], v[96:99]
	v_mfma_f32_16x16x32_bf16 v[92:95], v[144:147], v[208:211], v[92:95]
	v_mfma_f32_16x16x32_bf16 v[80:83], v[136:139], v[216:219], v[80:83]
	v_mfma_f32_16x16x32_bf16 v[76:79], v[144:147], v[216:219], v[76:79]
	s_setprio 0
	s_setprio 1
	v_mfma_f32_16x16x32_bf16 v[120:123], v[148:151], v[182:185], v[120:123]
	v_mfma_f32_16x16x32_bf16 v[116:119], v[156:159], v[182:185], v[116:119]
	v_mfma_f32_16x16x32_bf16 v[104:107], v[148:151], v[190:193], v[104:107]
	v_mfma_f32_16x16x32_bf16 v[100:103], v[156:159], v[190:193], v[100:103]
	v_mfma_f32_16x16x32_bf16 v[88:91], v[148:151], v[198:201], v[88:91]
	v_mfma_f32_16x16x32_bf16 v[84:87], v[156:159], v[198:201], v[84:87]
	v_mfma_f32_16x16x32_bf16 v[72:75], v[148:151], v[212:215], v[72:75]
	v_mfma_f32_16x16x32_bf16 v[68:71], v[156:159], v[212:215], v[68:71]
	v_mfma_f32_16x16x32_bf16 v[120:123], v[152:155], v[186:189], v[120:123]
	v_mfma_f32_16x16x32_bf16 v[116:119], v[160:163], v[186:189], v[116:119]
	v_mfma_f32_16x16x32_bf16 v[104:107], v[152:155], v[194:197], v[104:107]
	v_mfma_f32_16x16x32_bf16 v[100:103], v[160:163], v[194:197], v[100:103]
	v_mfma_f32_16x16x32_bf16 v[88:91], v[152:155], v[208:211], v[88:91]
	v_mfma_f32_16x16x32_bf16 v[84:87], v[160:163], v[208:211], v[84:87]
	v_mfma_f32_16x16x32_bf16 v[72:75], v[152:155], v[216:219], v[72:75]
	v_mfma_f32_16x16x32_bf16 v[68:71], v[160:163], v[216:219], v[68:71]
	s_setprio 0
	s_barrier
	s_add_i32 s61, s61, s27
	v_lshl_add_u64 v[228:229], s[0:1], 0, v[166:167]
	s_mov_b32 m0, s61
	ds_read_b128 v[182:185], v206 offset:16384
	ds_read_b128 v[186:189], v206 offset:17408
	ds_read_b128 v[190:193], v206 offset:18432
	ds_read_b128 v[194:197], v206 offset:19456
	ds_read_b128 v[198:201], v206 offset:20480
	ds_read_b128 v[208:211], v206 offset:21504
	ds_read_b128 v[212:215], v206 offset:22528
	ds_read_b128 v[216:219], v206 offset:23552
	global_load_lds_dwordx4 v[228:229], off
	s_add_i32 m0, s61, 0x2000
	s_add_u32 s78, s0, 0x40000
	v_lshl_add_u64 v[230:231], s[0:1], 0, v[170:171]
	s_addc_u32 s79, s1, 0
	s_add_i32 s61, s63, s27
	global_load_lds_dwordx4 v[230:231], off
	v_lshl_add_u64 v[232:233], s[78:79], 0, v[166:167]
	s_mov_b32 m0, s61
	v_lshl_add_u64 v[234:235], s[10:11], 0, v[168:169]
	global_load_lds_dwordx4 v[232:233], off
	v_lshl_add_u64 v[232:233], s[78:79], 0, v[170:171]
	s_add_i32 m0, s61, 0x2000
	s_nop 0
	global_load_lds_dwordx4 v[232:233], off
	v_lshl_add_u64 v[232:233], s[10:11], 0, v[164:165]
	s_mov_b32 m0, s19
	s_nop 0
	global_load_lds_dwordx4 v[232:233], off
	s_mov_b32 m0, s30
	s_nop 0
	global_load_lds_dwordx4 v[234:235], off
	s_waitcnt vmcnt(8)
	s_waitcnt lgkmcnt(0)
	s_barrier
; #define PG8_STAGE(bufoff, gbase, voff) do { _Pragma("unroll") for (int _i = 0; _i < 2; ++_i) \
;         __builtin_amdgcn_global_load_lds((const unsigned*)((const char*)(gbase) + (voff)[_i]), (PG8_LAS unsigned*)(lds + (bufoff) + ldsw + _i * 8192), 16, 0, 0); } while (0)
; #define PG8_LDA(dst, b, h) do { _Pragma("unroll") for (int m = 0; m < 4; ++m) _Pragma("unroll") for (int k = 0; k < 2; ++k) dst[m][k] = *(const PG8_LAS bf16x8*)(lds + PG8_SA(b, h) + aoff + m * 2048 + k * 1024); } while (0)
; #define PG8_LDB(dst, b, h) do { _Pragma("unroll") for (int n = 0; n < 2; ++n) _Pragma("unroll") for (int k = 0; k < 2; ++k) dst[n][k] = *(const PG8_LAS bf16x8*)(lds + PG8_SB(b, h) + boff + n * 2048 + k * 1024); } while (0)
; #define PG8_MMA(ai, bj, At, Bt) do { __builtin_amdgcn_s_setprio(1); _Pragma("unroll") for (int m = 0; m < 4; ++m) _Pragma("unroll") for (int n = 0; n < 2; ++n) _Pragma("unroll") for (int k = 0; k < 2; ++k) \
;         acc[ai][bj][m][n] = __builtin_amdgcn_mfma_f32_16x16x32_bf16(Bt[n][k], At[m][k], acc[ai][bj][m][n], 0, 0, 0); __builtin_amdgcn_s_setprio(0); } while (0)
; #define PG8_WAIT_V(n) asm volatile("s_waitcnt vmcnt(" #n ")" ::: "memory")
; #define PG8_WAIT_L(n) asm volatile("s_waitcnt lgkmcnt(" #n ")" ::: "memory")
; #define PG8_BAR __builtin_amdgcn_s_barrier()
; #define PG8_SCHED __builtin_amdgcn_sched_barrier(0)
; template <class Epi, class Sched, bool ALIGN_EPI = false, bool SP2 = false>
; __device__ __forceinline__ void gemm_phase(PG8_LAS unsigned char* lds, const Gemm g, const Sched& S, const Epi& E) {
;     ...
;             PG8_WAIT_V(8); PG8_WAIT_L(0); PG8_BAR; PG8_MMA(0, 0, At, B0); PG8_MMA(0, 1, At, B1); PG8_BAR; PG8_SCHED;
;             PG8_LDA(At, 0, 1); PG8_STAGE(PG8_SB(0, 0), b2, voffB); PG8_STAGE(PG8_SB(0, 1), b2 + hstep, voffB); PG8_STAGE(PG8_SA(0, 0), a2, voffA);
;             PG8_WAIT_V(8); PG8_WAIT_L(0); PG8_BAR; if (cur.half == 0) { PG8_MMA(1, 0, At, B0); PG8_MMA(1, 1, At, B1); } PG8_BAR; PG8_SCHED;
;             PG8_LDB(B0, 1, 0); PG8_LDB(B1, 1, 1); PG8_SCHED; PG8_LDA(At, 1, 0); PG8_STAGE(PG8_SA(0, 1), a2 + hstep, voffA);
;             PG8_WAIT_V(8); PG8_WAIT_L(0); PG8_BAR; PG8_MMA(0, 0, At, B0); PG8_MMA(0, 1, At, B1); PG8_BAR; PG8_SCHED;
	s_setprio 1
	s_waitcnt lgkmcnt(0)
	v_mfma_f32_16x16x32_bf16 v[64:67], v[132:135], v[182:185], v[64:67]
	v_mfma_f32_16x16x32_bf16 v[60:63], v[140:143], v[182:185], v[60:63]
	v_mfma_f32_16x16x32_bf16 v[48:51], v[132:135], v[190:193], v[48:51]
	v_mfma_f32_16x16x32_bf16 v[44:47], v[140:143], v[190:193], v[44:47]
	v_mfma_f32_16x16x32_bf16 v[32:35], v[132:135], v[198:201], v[32:35]
	v_mfma_f32_16x16x32_bf16 v[28:31], v[140:143], v[198:201], v[28:31]
	v_mfma_f32_16x16x32_bf16 v[16:19], v[132:135], v[212:215], v[16:19]
	v_mfma_f32_16x16x32_bf16 v[12:15], v[140:143], v[212:215], v[12:15]
	v_mfma_f32_16x16x32_bf16 v[64:67], v[136:139], v[186:189], v[64:67]
	v_mfma_f32_16x16x32_bf16 v[60:63], v[144:147], v[186:189], v[60:63]
	v_mfma_f32_16x16x32_bf16 v[48:51], v[136:139], v[194:197], v[48:51]
	v_mfma_f32_16x16x32_bf16 v[44:47], v[144:147], v[194:197], v[44:47]
	v_mfma_f32_16x16x32_bf16 v[32:35], v[136:139], v[208:211], v[32:35]
	v_mfma_f32_16x16x32_bf16 v[28:31], v[144:147], v[208:211], v[28:31]
	v_mfma_f32_16x16x32_bf16 v[16:19], v[136:139], v[216:219], v[16:19]
	v_mfma_f32_16x16x32_bf16 v[12:15], v[144:147], v[216:219], v[12:15]
	s_setprio 0
	s_setprio 1
	v_mfma_f32_16x16x32_bf16 v[56:59], v[148:151], v[182:185], v[56:59]
	v_mfma_f32_16x16x32_bf16 v[52:55], v[156:159], v[182:185], v[52:55]
	v_mfma_f32_16x16x32_bf16 v[40:43], v[148:151], v[190:193], v[40:43]
	v_mfma_f32_16x16x32_bf16 v[36:39], v[156:159], v[190:193], v[36:39]
	v_mfma_f32_16x16x32_bf16 v[24:27], v[148:151], v[198:201], v[24:27]
	v_mfma_f32_16x16x32_bf16 v[20:23], v[156:159], v[198:201], v[20:23]
	v_mfma_f32_16x16x32_bf16 v[8:11], v[148:151], v[212:215], v[8:11]
	v_mfma_f32_16x16x32_bf16 v[4:7], v[156:159], v[212:215], v[4:7]
	v_mfma_f32_16x16x32_bf16 v[56:59], v[152:155], v[186:189], v[56:59]
	v_mfma_f32_16x16x32_bf16 v[52:55], v[160:163], v[186:189], v[52:55]
	v_mfma_f32_16x16x32_bf16 v[40:43], v[152:155], v[194:197], v[40:43]
	v_mfma_f32_16x16x32_bf16 v[36:39], v[160:163], v[194:197], v[36:39]
	v_mfma_f32_16x16x32_bf16 v[24:27], v[152:155], v[208:211], v[24:27]
	v_mfma_f32_16x16x32_bf16 v[20:23], v[160:163], v[208:211], v[20:23]
	v_mfma_f32_16x16x32_bf16 v[8:11], v[152:155], v[216:219], v[8:11]
	v_mfma_f32_16x16x32_bf16 v[4:7], v[160:163], v[216:219], v[4:7]
	s_setprio 0
	s_barrier
	s_add_i32 s61, 0, 0x18000
	v_add_u32_e32 v2, s61, v203
	s_add_i32 s63, 0, 0x1c000
	ds_read_b128 v[132:135], v2
	ds_read_b128 v[136:139], v2 offset:1024
	ds_read_b128 v[140:143], v2 offset:2048
	ds_read_b128 v[144:147], v2 offset:3072
	v_add_u32_e32 v2, s63, v203
	ds_read_b128 v[148:151], v2
	ds_read_b128 v[152:155], v2 offset:1024
	ds_read_b128 v[156:159], v2 offset:2048
	ds_read_b128 v[160:163], v2 offset:3072
	s_add_u32 s10, s10, 0x40000
	s_addc_u32 s11, s11, 0
	s_mov_b32 m0, s31
	v_lshl_add_u64 v[236:237], s[10:11], 0, v[164:165]
	ds_read_b128 v[182:185], v206 offset:32768
	ds_read_b128 v[186:189], v206 offset:33792
	ds_read_b128 v[190:193], v206 offset:34816
	ds_read_b128 v[194:197], v206 offset:35840
	ds_read_b128 v[198:201], v206 offset:36864
	ds_read_b128 v[208:211], v206 offset:37888
	ds_read_b128 v[212:215], v206 offset:38912
	ds_read_b128 v[216:219], v206 offset:39936
	global_load_lds_dwordx4 v[236:237], off
	v_lshl_add_u64 v[236:237], s[10:11], 0, v[168:169]
	s_mov_b32 m0, s34
	s_nop 0
	global_load_lds_dwordx4 v[236:237], off
	s_waitcnt vmcnt(8)
	s_waitcnt lgkmcnt(0)
	s_barrier
	s_setprio 1
	s_waitcnt lgkmcnt(0)
	v_mfma_f32_16x16x32_bf16 v[128:131], v[132:135], v[182:185], v[128:131]
	v_mfma_f32_16x16x32_bf16 v[124:127], v[140:143], v[182:185], v[124:127]
	v_mfma_f32_16x16x32_bf16 v[112:115], v[132:135], v[190:193], v[112:115]
	v_mfma_f32_16x16x32_bf16 v[108:111], v[140:143], v[190:193], v[108:111]
	v_mfma_f32_16x16x32_bf16 v[96:99], v[132:135], v[198:201], v[96:99]
	v_mfma_f32_16x16x32_bf16 v[92:95], v[140:143], v[198:201], v[92:95]
	v_mfma_f32_16x16x32_bf16 v[80:83], v[132:135], v[212:215], v[80:83]
	v_mfma_f32_16x16x32_bf16 v[76:79], v[140:143], v[212:215], v[76:79]
	v_mfma_f32_16x16x32_bf16 v[128:131], v[136:139], v[186:189], v[128:131]
	v_mfma_f32_16x16x32_bf16 v[124:127], v[144:147], v[186:189], v[124:127]
	v_mfma_f32_16x16x32_bf16 v[112:115], v[136:139], v[194:197], v[112:115]
	v_mfma_f32_16x16x32_bf16 v[108:111], v[144:147], v[194:197], v[108:111]
	v_mfma_f32_16x16x32_bf16 v[96:99], v[136:139], v[208:211], v[96:99]
	v_mfma_f32_16x16x32_bf16 v[92:95], v[144:147], v[208:211], v[92:95]
	v_mfma_f32_16x16x32_bf16 v[80:83], v[136:139], v[216:219], v[80:83]
	v_mfma_f32_16x16x32_bf16 v[76:79], v[144:147], v[216:219], v[76:79]
	s_setprio 0
	s_setprio 1
	v_mfma_f32_16x16x32_bf16 v[120:123], v[148:151], v[182:185], v[120:123]
	v_mfma_f32_16x16x32_bf16 v[116:119], v[156:159], v[182:185], v[116:119]
	v_mfma_f32_16x16x32_bf16 v[104:107], v[148:151], v[190:193], v[104:107]
	v_mfma_f32_16x16x32_bf16 v[100:103], v[156:159], v[190:193], v[100:103]
	v_mfma_f32_16x16x32_bf16 v[88:91], v[148:151], v[198:201], v[88:91]
	v_mfma_f32_16x16x32_bf16 v[84:87], v[156:159], v[198:201], v[84:87]
	v_mfma_f32_16x16x32_bf16 v[72:75], v[148:151], v[212:215], v[72:75]
	v_mfma_f32_16x16x32_bf16 v[68:71], v[156:159], v[212:215], v[68:71]
	v_mfma_f32_16x16x32_bf16 v[120:123], v[152:155], v[186:189], v[120:123]
	v_mfma_f32_16x16x32_bf16 v[116:119], v[160:163], v[186:189], v[116:119]
	v_mfma_f32_16x16x32_bf16 v[104:107], v[152:155], v[194:197], v[104:107]
	v_mfma_f32_16x16x32_bf16 v[100:103], v[160:163], v[194:197], v[100:103]
	v_mfma_f32_16x16x32_bf16 v[88:91], v[152:155], v[208:211], v[88:91]
	v_mfma_f32_16x16x32_bf16 v[84:87], v[160:163], v[208:211], v[84:87]
	v_mfma_f32_16x16x32_bf16 v[72:75], v[152:155], v[216:219], v[72:75]
	v_mfma_f32_16x16x32_bf16 v[68:71], v[160:163], v[216:219], v[68:71]
	s_setprio 0
	s_barrier
; #define PG8_STAGE(bufoff, gbase, voff) do { _Pragma("unroll") for (int _i = 0; _i < 2; ++_i) \
;         __builtin_amdgcn_global_load_lds((const unsigned*)((const char*)(gbase) + (voff)[_i]), (PG8_LAS unsigned*)(lds + (bufoff) + ldsw + _i * 8192), 16, 0, 0); } while (0)
; #define PG8_LDA(dst, b, h) do { _Pragma("unroll") for (int m = 0; m < 4; ++m) _Pragma("unroll") for (int k = 0; k < 2; ++k) dst[m][k] = *(const PG8_LAS bf16x8*)(lds + PG8_SA(b, h) + aoff + m * 2048 + k * 1024); } while (0)
; #define PG8_MMA(ai, bj, At, Bt) do { __builtin_amdgcn_s_setprio(1); _Pragma("unroll") for (int m = 0; m < 4; ++m) _Pragma("unroll") for (int n = 0; n < 2; ++n) _Pragma("unroll") for (int k = 0; k < 2; ++k) \
;         acc[ai][bj][m][n] = __builtin_amdgcn_mfma_f32_16x16x32_bf16(Bt[n][k], At[m][k], acc[ai][bj][m][n], 0, 0, 0); __builtin_amdgcn_s_setprio(0); } while (0)
; #define PG8_WAIT_V(n) asm volatile("s_waitcnt vmcnt(" #n ")" ::: "memory")
; #define PG8_WAIT_L(n) asm volatile("s_waitcnt lgkmcnt(" #n ")" ::: "memory")
; #define PG8_BAR __builtin_amdgcn_s_barrier()
; #define PG8_SCHED __builtin_amdgcn_sched_barrier(0)
; template <class Epi, class Sched, bool ALIGN_EPI = false, bool SP2 = false>
; __device__ __forceinline__ void gemm_phase(PG8_LAS unsigned char* lds, const Gemm g, const Sched& S, const Epi& E) {
;     ...
;             PG8_LDA(At, 1, 1); PG8_STAGE(PG8_SB(1, 0), b3, voffB); PG8_STAGE(PG8_SB(1, 1), b3 + hstep, voffB); PG8_STAGE(PG8_SA(1, 0), a3, voffA);
;             PG8_WAIT_V(8); PG8_WAIT_L(0); PG8_BAR; if (cur.half == 0) { PG8_MMA(1, 0, At, B0); PG8_MMA(1, 1, At, B1); } PG8_BAR; PG8_SCHED;
;     ...
;         if constexpr (ALIGN_EPI) { if (wr == 0) PG8_BAR; }
	s_add_i32 s10, s61, s27
	v_lshl_add_u64 v[228:229], v[228:229], 0, s[42:43]
	s_mov_b32 m0, s10
	ds_read_b128 v[182:185], v206 offset:49152
	ds_read_b128 v[186:189], v206 offset:50176
	ds_read_b128 v[190:193], v206 offset:51200
	ds_read_b128 v[194:197], v206 offset:52224
	ds_read_b128 v[198:201], v206 offset:53248
	ds_read_b128 v[208:211], v206 offset:54272
	ds_read_b128 v[212:215], v206 offset:55296
	ds_read_b128 v[216:219], v206 offset:56320
	global_load_lds_dwordx4 v[228:229], off
	s_add_i32 m0, s10, 0x2000
	s_add_u32 s0, s0, 0x40080
	v_lshl_add_u64 v[228:229], v[230:231], 0, s[42:43]
	s_addc_u32 s1, s1, 0
	s_add_i32 s10, s63, s27
	global_load_lds_dwordx4 v[228:229], off
	v_lshl_add_u64 v[228:229], s[0:1], 0, v[166:167]
	s_mov_b32 m0, s10
	s_nop 0
	global_load_lds_dwordx4 v[228:229], off
	v_lshl_add_u64 v[228:229], s[0:1], 0, v[170:171]
	s_add_i32 m0, s10, 0x2000
	s_nop 0
	global_load_lds_dwordx4 v[228:229], off
	v_lshl_add_u64 v[228:229], v[232:233], 0, s[42:43]
	s_mov_b32 m0, s41
	s_nop 0
	global_load_lds_dwordx4 v[228:229], off
	v_lshl_add_u64 v[228:229], v[234:235], 0, s[42:43]
	s_mov_b32 m0, s71
	s_nop 0
	global_load_lds_dwordx4 v[228:229], off
	s_waitcnt vmcnt(8)
	s_waitcnt lgkmcnt(0)
	s_barrier
	s_setprio 1
	s_waitcnt lgkmcnt(0)
	v_mfma_f32_16x16x32_bf16 v[64:67], v[132:135], v[182:185], v[64:67]
	v_mfma_f32_16x16x32_bf16 v[60:63], v[140:143], v[182:185], v[60:63]
	v_mfma_f32_16x16x32_bf16 v[48:51], v[132:135], v[190:193], v[48:51]
	v_mfma_f32_16x16x32_bf16 v[44:47], v[140:143], v[190:193], v[44:47]
	v_mfma_f32_16x16x32_bf16 v[32:35], v[132:135], v[198:201], v[32:35]
	v_mfma_f32_16x16x32_bf16 v[28:31], v[140:143], v[198:201], v[28:31]
	v_mfma_f32_16x16x32_bf16 v[16:19], v[132:135], v[212:215], v[16:19]
	v_mfma_f32_16x16x32_bf16 v[12:15], v[140:143], v[212:215], v[12:15]
	v_mfma_f32_16x16x32_bf16 v[64:67], v[136:139], v[186:189], v[64:67]
	v_mfma_f32_16x16x32_bf16 v[60:63], v[144:147], v[186:189], v[60:63]
	v_mfma_f32_16x16x32_bf16 v[48:51], v[136:139], v[194:197], v[48:51]
	v_mfma_f32_16x16x32_bf16 v[44:47], v[144:147], v[194:197], v[44:47]
	v_mfma_f32_16x16x32_bf16 v[32:35], v[136:139], v[208:211], v[32:35]
	v_mfma_f32_16x16x32_bf16 v[28:31], v[144:147], v[208:211], v[28:31]
	v_mfma_f32_16x16x32_bf16 v[16:19], v[136:139], v[216:219], v[16:19]
	v_mfma_f32_16x16x32_bf16 v[12:15], v[144:147], v[216:219], v[12:15]
	s_setprio 0
	s_setprio 1
	v_mfma_f32_16x16x32_bf16 v[56:59], v[148:151], v[182:185], v[56:59]
	v_mfma_f32_16x16x32_bf16 v[52:55], v[156:159], v[182:185], v[52:55]
	v_mfma_f32_16x16x32_bf16 v[40:43], v[148:151], v[190:193], v[40:43]
	v_mfma_f32_16x16x32_bf16 v[36:39], v[156:159], v[190:193], v[36:39]
	v_mfma_f32_16x16x32_bf16 v[24:27], v[148:151], v[198:201], v[24:27]
	v_mfma_f32_16x16x32_bf16 v[20:23], v[156:159], v[198:201], v[20:23]
	v_mfma_f32_16x16x32_bf16 v[8:11], v[148:151], v[212:215], v[8:11]
	v_mfma_f32_16x16x32_bf16 v[4:7], v[156:159], v[212:215], v[4:7]
	v_mfma_f32_16x16x32_bf16 v[56:59], v[152:155], v[186:189], v[56:59]
	v_mfma_f32_16x16x32_bf16 v[52:55], v[160:163], v[186:189], v[52:55]
	v_mfma_f32_16x16x32_bf16 v[40:43], v[152:155], v[194:197], v[40:43]
	v_mfma_f32_16x16x32_bf16 v[36:39], v[160:163], v[194:197], v[36:39]
	v_mfma_f32_16x16x32_bf16 v[24:27], v[152:155], v[208:211], v[24:27]
	v_mfma_f32_16x16x32_bf16 v[20:23], v[160:163], v[208:211], v[20:23]
	v_mfma_f32_16x16x32_bf16 v[8:11], v[152:155], v[216:219], v[8:11]
	v_mfma_f32_16x16x32_bf16 v[4:7], v[160:163], v[216:219], v[4:7]
	s_setprio 0
	s_barrier
	s_add_i32 s39, s39, 2
	s_add_u32 s8, s8, 0x100
	s_addc_u32 s9, s9, 0
	s_add_u32 s36, s36, 0x100
	s_addc_u32 s38, s38, 0
	s_cmp_gt_u32 s39, 13
	s_cbranch_scc0 .LBB0_395
	s_and_b64 vcc, exec, s[58:59]
	s_cbranch_vccz .LBB0_398
	s_barrier

; #define PG8_BAR __builtin_amdgcn_s_barrier()
; template <class Epi, class Sched, bool ALIGN_EPI = false, bool SP2 = false>
; __device__ __forceinline__ void gemm_phase(PG8_LAS unsigned char* lds, const Gemm g, const Sched& S, const Epi& E) {
;     ...
;         cur = nxt; cA = nA; cB = nB; ++ui;
;         if constexpr (ALIGN_EPI) { if (wr == 1) PG8_BAR; }
.LBB0_543:
	s_andn2_b64 vcc, exec, s[64:65]
	s_mov_b64 s[0:1], -1
	s_cbranch_vccnz .LBB0_391
	s_andn2_b64 vcc, exec, s[56:57]
	s_cbranch_vccnz .LBB0_390
	s_barrier
	s_branch .LBB0_390

; #define PG8_LAS __attribute__((address_space(3)))
; #define PG8_STAGE(bufoff, gbase, voff) do { _Pragma("unroll") for (int _i = 0; _i < 2; ++_i) \
;         __builtin_amdgcn_global_load_lds((const unsigned*)((const char*)(gbase) + (voff)[_i]), (PG8_LAS unsigned*)(lds + (bufoff) + ldsw + _i * 8192), 16, 0, 0); } while (0)
; #define PG8_WAIT_V(n) asm volatile("s_waitcnt vmcnt(" #n ")" ::: "memory")
; #define PG8_BAR __builtin_amdgcn_s_barrier()
; template <class Epi, class Sched, bool ALIGN_EPI = false, bool SP2 = false>
; __device__ __forceinline__ void gemm_phase(PG8_LAS unsigned char* lds, const Gemm g, const Sched& S, const Epi& E) {
;     ...
;     if constexpr (SP2) {
;         PG8_STAGE(PG8_SB(0, 0), cB, voffB); PG8_STAGE(PG8_SB(0, 1), cB + hstep, voffB); PG8_STAGE(PG8_SA(0, 0), cA, voffA); PG8_STAGE(PG8_SA(0, 1), cA + hstep, voffA);
;         if (wr == 1) PG8_BAR;
;         PG8_WAIT_V(2); PG8_BAR;
;         if constexpr (Epi::ROWSCALE) stage_row_factors(rowp_, (PG8_LAS float*)E.rsl, tid);
;         PG8_STAGE(PG8_SB(1, 0), cB + kstep, voffB); PG8_STAGE(PG8_SA(1, 0), cA + kstep, voffA); PG8_STAGE(PG8_SB(1, 1), cB + hstep + kstep, voffB);
;         PG8_WAIT_V(6); PG8_BAR;
.LBB0_1469:
	s_waitcnt vmcnt(2)
	v_mov_b32_e32 v137, v3
	v_mov_b32_e32 v133, v3
	v_mov_b32_e32 v135, v3
	v_lshl_add_u64 v[12:13], s[0:1], 0, v[2:3]
	v_lshl_add_u64 v[14:15], s[0:1], 0, v[136:137]
	v_lshl_add_u64 v[10:11], s[26:27], 0, v[132:133]
	v_lshl_add_u64 v[8:9], s[26:27], 0, v[134:135]
	s_barrier
	s_and_saveexec_b64 s[16:17], s[4:5]
	s_cbranch_execz .LBB0_1471
	s_waitcnt vmcnt(2)
	v_mov_b32_e32 v24, v5
	v_mov_b32_e32 v25, v6
	v_mov_b32_e32 v5, v7
	v_pk_add_f32 v[4:5], v[24:25], v[4:5]
	s_nop 0
	v_add_f32_e32 v4, v4, v5
	v_fmamk_f32 v4, v4, 0x3a800000, v226
	v_rsq_f32_e32 v4, v4
	v_lshl_add_u32 v5, v16, 2, 0
	v_add_u32_e32 v5, 0x20400, v5
	ds_write_b32 v5, v4
.LBB0_1471:
	s_or_b64 exec, exec, s[16:17]
	s_or_b32 s16, s13, s19
	s_mov_b32 s13, s37
	s_lshl_b64 s[4:5], s[12:13], 20
	s_add_u32 s4, s10, s4
	s_addc_u32 s5, s11, s5
	s_mul_i32 s16, s16, 0x160000
	s_sub_u32 s4, s4, s16
	s_subb_u32 s5, s5, 0
	s_lshl_b32 s12, s29, 5
	s_and_b32 s17, s12, 0x60
	s_add_i32 m0, s15, 0x18000
	s_waitcnt vmcnt(2)
	v_lshl_add_u64 v[4:5], v[12:13], 0, s[42:43]
	s_lshl_b32 s16, s28, 13
	s_lshl_b32 s19, s17, 7
	global_load_lds_dwordx4 v[4:5], off
	v_lshl_add_u64 v[4:5], v[14:15], 0, s[42:43]
	s_add_i32 m0, s15, 0x1a000
	s_add_i32 s41, s15, 0x8000
	s_add_i32 s60, s15, 0xa000
	global_load_lds_dwordx4 v[4:5], off
	v_lshl_add_u64 v[4:5], v[10:11], 0, s[42:43]
	s_mov_b32 m0, s41
	s_add_u32 s12, s0, 0x40080
	global_load_lds_dwordx4 v[4:5], off
	v_lshl_add_u64 v[4:5], v[8:9], 0, s[42:43]
	s_mov_b32 m0, s60
	s_addc_u32 s13, s1, 0
	global_load_lds_dwordx4 v[4:5], off
	s_add_i32 m0, s15, 0x1c000
	v_lshl_add_u64 v[4:5], s[12:13], 0, v[2:3]
	global_load_lds_dwordx4 v[4:5], off
	v_lshl_add_u64 v[4:5], s[12:13], 0, v[136:137]
	s_add_i32 m0, s15, 0x1e000
	v_lshlrev_b32_e32 v8, 2, v16
	global_load_lds_dwordx4 v[4:5], off
	v_lshrrev_b32_e32 v5, 1, v16
	v_and_b32_e32 v4, 15, v16
	v_and_b32_e32 v5, 24, v5
	v_lshl_or_b32 v146, s28, 6, v4
	v_lshlrev_b32_e32 v6, 1, v5
	v_lshl_or_b32 v4, v4, 6, v6
	v_lshlrev_b32_e32 v6, 2, v146
	v_and_b32_e32 v7, 32, v6
	v_and_b32_e32 v8, 32, v8
	v_bitop3_b32 v7, v4, s16, v7 bitop3:0xde
	v_bitop3_b32 v147, v4, s19, v8 bitop3:0xde
	v_lshlrev_b32_e32 v4, 14, v17
	v_and_b32_e32 v4, 0xffff8000, v4
	v_or_b32_e32 v149, s17, v5
	v_lshl_add_u32 v4, v18, 11, v4
	v_and_b32_e32 v5, 1, v17
	v_lshl_or_b32 v4, v5, 6, v4
	v_lshl_add_u32 v138, v19, 1, v4
	v_lshlrev_b32_e32 v4, 14, v20
	v_and_b32_e32 v4, 0xffff8000, v4
	s_waitcnt vmcnt(6)
	s_cmpk_lt_u32 s18, 0x100
	v_lshl_add_u32 v4, v21, 11, v4
	v_and_b32_e32 v5, 1, v20
	s_cselect_b64 s[12:13], -1, 0
	s_add_i32 s16, 0, 0x20400
	v_lshl_or_b32 v4, v5, 6, v4
	v_add_u32_e32 v148, s16, v6
	v_mov_b32_e32 v139, v3
	v_lshl_add_u32 v140, v22, 1, v4
	v_mov_b32_e32 v141, v3
	s_mov_b32 s61, 0
	v_add_u32_e32 v150, 0, v7
	s_barrier
	s_branch .LBB0_1474
